# v039 + agent-scope write-through (sc1) on prep XfV/XfA and fold Wf stores: dirty lines drain during the kernels instead of in the end-of-kernel L2 flush
# speedup vs baseline: 1.0261x; 1.0261x over previous
.LBB0_9:
	s_or_b64 exec, exec, s[6:7]
	v_lshlrev_b32_e32 v4, 3, v70
	v_and_b32_e32 v2, 4, v2
	v_and_b32_e32 v5, 28, v0
	s_lshl_b32 s0, s3, 3
	s_lshl_b32 s1, s2, s12
	v_bitop3_b32 v2, v4, v5, v2 bitop3:0x36
	s_add_i32 s0, s0, s1
	v_and_b32_e32 v3, 31, v0
	v_lshlrev_b32_e32 v16, 2, v2
	s_ashr_i32 s1, s0, 31
	v_lshl_or_b32 v17, v3, 7, v16
	s_lshl_b64 s[0:1], s[0:1], 15
	ds_read_b128 v[2:5], v17
	ds_read_b128 v[6:9], v17 offset:4096
	s_add_u32 s0, s4, s0
	s_addc_u32 s1, s5, s1
	s_lshl_b32 s2, s10, 12
	s_add_u32 s0, s0, s2
	s_addc_u32 s1, s1, 0
	v_lshl_or_b32 v10, v70, 10, v54
	s_waitcnt lgkmcnt(1)
	global_store_dwordx4 v10, v[2:5], s[0:1] sc1
	s_movk_i32 s2, 0xc0
	v_and_or_b32 v1, v0, s2, v1
	s_waitcnt lgkmcnt(0)
	v_pk_mov_b32 v[4:5], v[8:9], v[8:9] op_sel:[1,0]
	v_pk_mov_b32 v[2:3], v[6:7], v[6:7] op_sel:[1,0]
	ds_read_b128 v[6:9], v17 offset:8192
	v_lshlrev_b32_e32 v18, 4, v1
	v_or_b32_e32 v1, 0x8000, v18
	global_store_dwordx4 v1, v[2:5], s[0:1] sc1
	ds_read_b128 v[2:5], v17 offset:12288
	s_waitcnt lgkmcnt(1)
	v_mov_b32_e32 v10, v6
	v_mov_b32_e32 v11, v7
	v_or_b32_e32 v1, 0x10000, v18
	global_store_dwordx4 v1, v[8:11], s[0:1] sc1
	ds_read_b128 v[8:11], v17 offset:16384
	ds_read_b128 v[12:15], v17 offset:20480
	s_waitcnt lgkmcnt(2)
	v_pk_mov_b32 v[6:7], v[2:3], v[2:3] op_sel:[1,0]
	v_pk_mov_b32 v[4:5], v[4:5], v[4:5] op_sel:[1,0]
	v_or_b32_e32 v1, 0x18000, v18
	global_store_dwordx4 v1, v[4:7], s[0:1] sc1
	v_or_b32_e32 v1, 0x20000, v18
	s_waitcnt lgkmcnt(1)
	global_store_dwordx4 v1, v[8:11], s[0:1] sc1
	s_waitcnt lgkmcnt(0)
	v_pk_mov_b32 v[4:5], v[14:15], v[14:15] op_sel:[1,0]
	v_pk_mov_b32 v[2:3], v[12:13], v[12:13] op_sel:[1,0]
	v_or_b32_e32 v1, 0x28000, v18
	v_lshlrev_b32_e32 v0, 7, v0
	s_movk_i32 s2, 0x7000
	global_store_dwordx4 v1, v[2:5], s[0:1] sc1
	ds_read_b128 v[2:5], v17 offset:24576
	v_or3_b32 v0, v0, v16, s2
	ds_read_b128 v[6:9], v0
	s_waitcnt lgkmcnt(1)
	v_mov_b32_e32 v0, v4
	v_mov_b32_e32 v1, v5
	v_or_b32_e32 v4, 0x30000, v18
	global_store_dwordx4 v4, v[0:3], s[0:1] sc1
	v_or_b32_e32 v4, 0x38000, v18
	s_waitcnt lgkmcnt(0)
	v_pk_mov_b32 v[2:3], v[6:7], v[6:7] op_sel:[1,0]
	v_pk_mov_b32 v[0:1], v[8:9], v[8:9] op_sel:[1,0]
	global_store_dwordx4 v4, v[0:3], s[0:1] sc1
	s_endpgm

.LBB1_65:
	s_or_b64 exec, exec, s[10:11]
	v_lshrrev_b32_e32 v20, 2, v58
	v_and_b32_e32 v19, 2, v52
	v_and_b32_e32 v20, 28, v20
	v_or_b32_e32 v21, 0x1880, v20
	v_lshlrev_b32_e32 v24, 5, v19
	v_or_b32_e32 v25, v21, v24
	s_waitcnt lgkmcnt(0)
	s_barrier
	ds_read_b32 v25, v25
	v_or_b32_e32 v26, 1, v52
	v_or_b32_e32 v20, 0x1800, v20
	v_lshlrev_b32_e32 v27, 5, v26
	v_or_b32_e32 v24, v20, v24
	v_or_b32_e32 v21, v21, v27
	v_or_b32_e32 v20, v20, v27
	ds_read_b32 v24, v24
	ds_read_b32 v21, v21
	ds_read_b32 v20, v20
	v_lshlrev_b32_e32 v22, 2, v58
	v_or_b32_e32 v23, 0x800, v22
	s_waitcnt vmcnt(1) lgkmcnt(3)
	v_mul_f32_e32 v25, v57, v25
	v_lshlrev_b32_e32 v19, 9, v19
	s_load_dwordx2 s[0:1], s[0:1], 0x48
	v_or_b32_e32 v27, v22, v19
	s_waitcnt vmcnt(0) lgkmcnt(0)
	v_fma_f32 v24, -v25, v24, v56
	v_or_b32_e32 v19, v23, v19
	ds_write_b32 v19, v24
	v_mul_f32_e32 v19, v57, v21
	v_lshlrev_b32_e32 v21, 9, v26
	v_or_b32_e32 v22, v22, v21
	v_and_b32_e32 v48, 63, v0
	ds_write_b32 v22, v19
	v_fma_f32 v19, -v19, v20, v56
	v_or_b32_e32 v20, v23, v21
	ds_write_b32 v20, v19
	v_add_u32_e32 v38, v52, v18
	v_lshlrev_b32_e32 v18, 4, v48
	v_mov_b32_e32 v19, 0
	v_lshl_add_u64 v[40:41], s[0:1], 0, v[18:19]
	v_or_b32_e32 v18, v55, v54
	v_lshlrev_b32_e32 v49, 2, v18
	v_ashrrev_i32_e32 v39, 31, v38
	ds_write_b32 v27, v25
	s_waitcnt lgkmcnt(0)
	s_barrier
	ds_read_b128 v[18:21], v49
	v_lshlrev_b64 v[22:23], 10, v[38:39]
	v_lshl_add_u64 v[42:43], v[40:41], 0, v[22:23]
	ds_read_b128 v[22:25], v49 offset:16
	s_lshl_b32 s5, s4, 2
	s_waitcnt lgkmcnt(1)
	v_pk_mul_f32 v[18:19], v[14:15], v[18:19]
	v_pk_mul_f32 v[20:21], v[16:17], v[20:21]
	s_ashr_i32 s13, s2, 31
	v_cvt_pk_bf16_f32 v18, v18, v19
	v_cvt_pk_bf16_f32 v19, v20, v21
	s_waitcnt lgkmcnt(0)
	v_pk_mul_f32 v[20:21], v[6:7], v[22:23]
	v_pk_mul_f32 v[22:23], v[8:9], v[24:25]
	s_mul_i32 s0, s4, 0xc0
	v_cvt_pk_bf16_f32 v20, v20, v21
	v_cvt_pk_bf16_f32 v21, v22, v23
	s_mul_hi_i32 s1, s5, 48
	s_add_u32 s0, s0, s2
	ds_read_b128 v[22:25], v49 offset:2048
	s_addc_u32 s1, s1, s13
	s_lshl_b64 s[0:1], s[0:1], 15
	v_lshl_add_u64 v[26:27], v[42:43], 0, s[0:1]
	global_store_dwordx4 v[26:27], v[18:21], off sc1
	ds_read_b128 v[18:21], v49 offset:2064
	s_waitcnt lgkmcnt(1)
	v_mul_f32_e32 v26, v15, v23
	v_fmac_f32_e32 v26, v14, v22
	v_fmac_f32_e32 v26, v16, v24
	v_fmac_f32_e32 v26, v17, v25
	s_waitcnt lgkmcnt(0)
	v_fmac_f32_e32 v26, v6, v18
	v_fmac_f32_e32 v26, v7, v19
	v_fmac_f32_e32 v26, v8, v20
	ds_read_b128 v[22:25], v49 offset:512
	v_fmac_f32_e32 v26, v9, v21
	ds_read_b128 v[18:21], v49 offset:528
	s_or_b32 s6, s5, 1
	s_mul_hi_i32 s7, s6, 48
	s_mul_i32 s6, s6, 48
	s_add_u32 s6, s6, s2
	s_waitcnt lgkmcnt(1)
	v_pk_mul_f32 v[22:23], v[14:15], v[22:23]
	v_pk_mul_f32 v[24:25], v[16:17], v[24:25]
	s_waitcnt lgkmcnt(0)
	v_pk_mul_f32 v[18:19], v[6:7], v[18:19]
	s_addc_u32 s7, s7, s13
	v_cvt_pk_bf16_f32 v22, v22, v23
	v_cvt_pk_bf16_f32 v23, v24, v25
	v_cvt_pk_bf16_f32 v24, v18, v19
	v_pk_mul_f32 v[18:19], v[8:9], v[20:21]
	s_lshl_b64 s[6:7], s[6:7], 15
	v_cvt_pk_bf16_f32 v25, v18, v19
	v_lshl_add_u64 v[18:19], v[42:43], 0, s[6:7]
	v_add_f32_e32 v50, 0, v26
	ds_read_b128 v[26:29], v49 offset:1024
	global_store_dwordx4 v[18:19], v[22:25], off sc1
	ds_read_b128 v[22:25], v49 offset:2560
	ds_read_b128 v[18:21], v49 offset:2576
	ds_read_b128 v[30:33], v49 offset:1040
	s_or_b32 s10, s5, 2
	s_mul_hi_i32 s11, s10, 48
	s_mul_i32 s10, s10, 48
	s_add_u32 s10, s10, s2
	s_waitcnt lgkmcnt(3)
	v_pk_mul_f32 v[26:27], v[14:15], v[26:27]
	v_pk_mul_f32 v[28:29], v[16:17], v[28:29]
	s_addc_u32 s11, s11, s13
	v_cvt_pk_bf16_f32 v26, v26, v27
	v_cvt_pk_bf16_f32 v27, v28, v29
	s_waitcnt lgkmcnt(0)
	v_pk_mul_f32 v[28:29], v[6:7], v[30:31]
	v_pk_mul_f32 v[30:31], v[8:9], v[32:33]
	s_lshl_b64 s[10:11], s[10:11], 15
	v_cvt_pk_bf16_f32 v28, v28, v29
	v_cvt_pk_bf16_f32 v29, v30, v31
	v_lshl_add_u64 v[34:35], v[42:43], 0, s[10:11]
	ds_read_b128 v[30:33], v49 offset:1536
	global_store_dwordx4 v[34:35], v[26:29], off sc1
	ds_read_b128 v[26:29], v49 offset:1552
	s_or_b32 s5, s5, 3
	s_mul_hi_i32 s14, s5, 48
	s_mul_i32 s5, s5, 48
	s_add_u32 s12, s5, s2
	s_addc_u32 s13, s14, s13
	s_waitcnt lgkmcnt(1)
	v_pk_mul_f32 v[30:31], v[14:15], v[30:31]
	v_pk_mul_f32 v[32:33], v[16:17], v[32:33]
	s_waitcnt lgkmcnt(0)
	v_pk_mul_f32 v[26:27], v[6:7], v[26:27]
	v_pk_mul_f32 v[44:45], v[8:9], v[28:29]
	s_lshl_b64 s[12:13], s[12:13], 15
	v_add_u32_e32 v38, 4, v38
	v_cvt_pk_bf16_f32 v34, v30, v31
	v_cvt_pk_bf16_f32 v35, v32, v33
	v_cvt_pk_bf16_f32 v36, v26, v27
	v_cvt_pk_bf16_f32 v37, v44, v45
	v_lshl_add_u64 v[42:43], v[42:43], 0, s[12:13]
	v_add_lshl_u32 v71, v55, v54, 2
	v_ashrrev_i32_e32 v39, 31, v38
	ds_read_b128 v[30:33], v49 offset:3072
	ds_read_b128 v[26:29], v49 offset:3088
	global_store_dwordx4 v[42:43], v[34:37], off sc1
	ds_read_b128 v[34:37], v71 offset:256
	v_lshlrev_b64 v[38:39], 10, v[38:39]
	v_lshl_add_u64 v[46:47], v[40:41], 0, v[38:39]
	ds_read_b128 v[38:41], v71 offset:272
	v_lshlrev_b32_e32 v66, 2, v53
	s_waitcnt lgkmcnt(1)
	v_pk_mul_f32 v[34:35], v[10:11], v[34:35]
	v_pk_mul_f32 v[36:37], v[12:13], v[36:37]
	v_cvt_pk_bf16_f32 v34, v34, v35
	v_cvt_pk_bf16_f32 v35, v36, v37
	s_waitcnt lgkmcnt(0)
	v_pk_mul_f32 v[36:37], v[2:3], v[38:39]
	v_pk_mul_f32 v[42:43], v[4:5], v[40:41]
	ds_read_b128 v[38:41], v71 offset:2304
	v_cvt_pk_bf16_f32 v36, v36, v37
	v_cvt_pk_bf16_f32 v37, v42, v43
	v_lshl_add_u64 v[42:43], v[46:47], 0, s[0:1]
	global_store_dwordx4 v[42:43], v[34:37], off sc1
	ds_read_b128 v[34:37], v71 offset:2320
	s_waitcnt lgkmcnt(1)
	v_mul_f32_e32 v51, v11, v39
	v_fmac_f32_e32 v51, v10, v38
	v_fmac_f32_e32 v51, v12, v40
	v_fmac_f32_e32 v51, v13, v41
	s_waitcnt lgkmcnt(0)
	v_fmac_f32_e32 v51, v2, v34
	v_fmac_f32_e32 v51, v3, v35
	v_fmac_f32_e32 v51, v4, v36
	ds_read_b128 v[38:41], v71 offset:768
	v_fmac_f32_e32 v51, v5, v37
	ds_read_b128 v[34:37], v71 offset:784
	s_movk_i32 s0, 0x1000
	v_add_f32_e32 v69, v50, v51
	s_waitcnt lgkmcnt(1)
	v_pk_mul_f32 v[38:39], v[10:11], v[38:39]
	v_pk_mul_f32 v[40:41], v[12:13], v[40:41]
	s_waitcnt lgkmcnt(0)
	v_pk_mul_f32 v[34:35], v[2:3], v[34:35]
	v_pk_mul_f32 v[42:43], v[4:5], v[36:37]
	v_cvt_pk_bf16_f32 v38, v38, v39
	v_cvt_pk_bf16_f32 v39, v40, v41
	v_cvt_pk_bf16_f32 v40, v34, v35
	ds_read_b128 v[34:37], v71 offset:1280
	v_cvt_pk_bf16_f32 v41, v42, v43
	v_lshl_add_u64 v[42:43], v[46:47], 0, s[6:7]
	global_store_dwordx4 v[42:43], v[38:41], off sc1
	ds_read_b128 v[38:41], v71 offset:1296
	s_waitcnt lgkmcnt(1)
	v_pk_mul_f32 v[34:35], v[10:11], v[34:35]
	v_pk_mul_f32 v[36:37], v[12:13], v[36:37]
	v_cvt_pk_bf16_f32 v34, v34, v35
	v_cvt_pk_bf16_f32 v35, v36, v37
	s_waitcnt lgkmcnt(0)
	v_pk_mul_f32 v[36:37], v[2:3], v[38:39]
	v_pk_mul_f32 v[42:43], v[4:5], v[40:41]
	v_cvt_pk_bf16_f32 v36, v36, v37
	v_cvt_pk_bf16_f32 v37, v42, v43
	v_lshl_add_u64 v[42:43], v[46:47], 0, s[10:11]
	ds_read_b128 v[38:41], v71 offset:1792
	global_store_dwordx4 v[42:43], v[34:37], off sc1
	ds_read_b128 v[34:37], v71 offset:1808
	v_lshl_add_u64 v[46:47], v[46:47], 0, s[12:13]
	s_waitcnt lgkmcnt(1)
	v_pk_mul_f32 v[38:39], v[10:11], v[38:39]
	v_pk_mul_f32 v[40:41], v[12:13], v[40:41]
	s_waitcnt lgkmcnt(0)
	v_pk_mul_f32 v[34:35], v[2:3], v[34:35]
	v_cvt_pk_bf16_f32 v42, v38, v39
	v_cvt_pk_bf16_f32 v44, v34, v35
	v_pk_mul_f32 v[34:35], v[4:5], v[36:37]
	v_cvt_pk_bf16_f32 v43, v40, v41
	v_cvt_pk_bf16_f32 v45, v34, v35
	ds_read_b128 v[38:41], v49 offset:3584
	ds_read_b128 v[34:37], v49 offset:3600
	global_store_dwordx4 v[46:47], v[42:45], off sc1
	s_nop 1
	v_mbcnt_lo_u32_b32 v42, -1, 0
	v_mbcnt_hi_u32_b32 v42, -1, v42
	v_and_b32_e32 v44, 64, v42
	v_xor_b32_e32 v43, 32, v42
	v_add_u32_e32 v44, 64, v44
	v_cmp_lt_i32_e32 vcc, v43, v44
	s_nop 1
	v_cndmask_b32_e32 v42, v42, v43, vcc
	v_lshlrev_b32_e32 v68, 2, v42
	v_lshlrev_b32_e32 v42, 9, v52
	v_cmp_gt_u32_e32 vcc, 32, v48
	v_or3_b32 v67, v42, v66, s0
	ds_read_b128 v[62:65], v71 offset:2816
	ds_read_b128 v[58:61], v71 offset:2832
	ds_read_b128 v[54:57], v71 offset:3328
	ds_read_b128 v[50:53], v71 offset:3344
	ds_read_b128 v[46:49], v71 offset:3840
	ds_read_b128 v[42:45], v71 offset:3856
	ds_bpermute_b32 v70, v68, v69
	s_and_saveexec_b64 s[0:1], vcc
	s_cbranch_execz .LBB1_67
	s_waitcnt lgkmcnt(0)
	v_add_f32_e32 v69, v69, v70
	ds_write_b32 v67, v69
